# v027 + P3 pair-tile PV MFMAs accumulate in place (latch copies removed) + P0 silu loop software-pipelined
# speedup vs baseline: 1.0187x; 1.0187x over previous
.LBB0_7:
	s_or_b64 exec, exec, s[2:3]
	s_load_dwordx16 s[4:19], s[0:1], 0x0
	s_lshl_b32 s72, s65, 3
	v_and_b32_e32 v174, 63, v0
	s_waitcnt lgkmcnt(0)
	v_writelane_b32 v252, s4, 13
	s_nop 1
	v_writelane_b32 v252, s5, 14
	v_writelane_b32 v252, s6, 15
	v_writelane_b32 v252, s7, 16
	v_writelane_b32 v252, s8, 17
	v_writelane_b32 v252, s9, 18
	v_writelane_b32 v252, s10, 19
	v_writelane_b32 v252, s11, 20
	v_writelane_b32 v252, s12, 21
	v_writelane_b32 v252, s13, 22
	v_writelane_b32 v252, s14, 23
	v_writelane_b32 v252, s15, 24
	v_writelane_b32 v252, s16, 25
	v_writelane_b32 v252, s17, 26
	v_writelane_b32 v252, s18, 27
	v_writelane_b32 v252, s19, 28
	s_load_dwordx16 s[4:19], s[0:1], 0x40
	s_lshr_b32 s0, s20, 6
	s_waitcnt lgkmcnt(0)
	v_writelane_b32 v252, s4, 29
	s_nop 1
	v_writelane_b32 v252, s5, 30
	v_writelane_b32 v252, s6, 31
	v_writelane_b32 v252, s7, 32
	v_writelane_b32 v252, s8, 33
	v_writelane_b32 v252, s9, 34
	v_writelane_b32 v252, s10, 35
	v_writelane_b32 v252, s11, 36
	v_writelane_b32 v252, s12, 37
	v_writelane_b32 v252, s13, 38
	v_writelane_b32 v252, s14, 39
	v_writelane_b32 v252, s15, 40
	v_writelane_b32 v252, s16, 41
	v_writelane_b32 v252, s17, 42
	v_writelane_b32 v252, s18, 43
	v_writelane_b32 v252, s19, 44
	v_writelane_b32 v252, s20, 45
	v_writelane_b32 v252, s0, 46
	s_add_i32 s0, s72, s0
	v_writelane_b32 v252, s0, 47
	s_lshl_b32 s0, s59, 3
	s_add_u32 s92, s70, 0x100000
	v_writelane_b32 v252, s0, 48
	s_addc_u32 s0, s71, 0
	s_add_u32 s6, s70, 0x300000
	s_addc_u32 s7, s71, 0
	s_add_u32 s40, s70, 0x900000
	s_addc_u32 s41, s71, 0
	s_add_u32 s38, s70, 0xb00000
	s_addc_u32 s39, s71, 0
	v_writelane_b32 v252, s0, 49
	s_add_u32 s0, s70, 0xf00000
	s_addc_u32 s1, s71, 0
	s_add_u32 s61, s70, 0x1100000
	s_addc_u32 s62, s71, 0
	s_add_u32 s33, s70, 0x11100000
	s_addc_u32 s60, s71, 0
	s_add_u32 s8, s70, 0x600000
	s_addc_u32 s9, s71, 0
	v_writelane_b32 v252, s0, 51
	s_cmp_lt_i32 s68, 1
	s_nop 0
	v_writelane_b32 v252, s1, 52
	s_cselect_b64 s[0:1], -1, 0
	s_cmp_gt_i32 s69, 0
	s_cselect_b64 s[2:3], -1, 0
	s_and_b64 s[0:1], s[0:1], s[2:3]
	v_writelane_b32 v252, s70, 53
	s_andn2_b64 vcc, exec, s[0:1]
	s_nop 0
	v_writelane_b32 v252, s71, 54
	s_cbranch_vccnz .LBB0_127
	s_add_u32 s10, s70, 0x8400
	s_addc_u32 s11, s71, 0
	s_add_u32 s12, s70, 0x8420
	s_addc_u32 s13, s71, 0
	s_cmpk_gt_u32 s58, 0xbf
	s_mov_b64 s[2:3], -1
	s_cbranch_scc1 .LBB0_18
	v_readlane_b32 s16, v252, 13
	v_lshlrev_b32_e32 v2, 2, v0
	v_mov_b32_e32 v3, 0
	v_readlane_b32 s18, v252, 15
	v_readlane_b32 s19, v252, 16
	v_or_b32_e32 v40, 0x200, v0
	v_lshl_add_u32 v4, v0, 7, 0
	v_lshl_add_u64 v[2:3], s[18:19], 0, v[2:3]
	s_mov_b64 s[0:1], 0x1000
	v_and_b32_e32 v7, 0xffff, v40
	s_mov_b32 s34, s59
	v_lshl_add_u64 v[2:3], v[2:3], 0, s[0:1]
	v_or_b32_e32 v1, 0x600, v0
	v_add_u32_e32 v5, 0x10004, v4
	v_add_u32_e32 v6, 4, v4
	v_lshl_add_u32 v7, v7, 7, 0
	s_movk_i32 s16, 0xff80
	s_mov_b64 s[14:15], 0x2000
	v_readlane_b32 s17, v252, 14
	v_readlane_b32 s20, v252, 17
	v_readlane_b32 s21, v252, 18
	v_readlane_b32 s22, v252, 19
	v_readlane_b32 s23, v252, 20
	v_readlane_b32 s24, v252, 21
	v_readlane_b32 s25, v252, 22
	v_readlane_b32 s26, v252, 23
	v_readlane_b32 s27, v252, 24
	v_readlane_b32 s28, v252, 25
	v_readlane_b32 s29, v252, 26
	v_readlane_b32 s30, v252, 27
	v_readlane_b32 s31, v252, 28
	global_load_dword v44, v[2:3], off offset:-4096
	global_load_dword v45, v[2:3], off offset:-2048
	global_load_dword v46, v[2:3], off
	global_load_dword v47, v[2:3], off offset:2048
.LBB0_10:
	s_waitcnt vmcnt(0)
	v_mov_b32_e32 v8, v44
	v_mov_b32_e32 v9, v45
	v_mov_b32_e32 v10, v46
	v_mov_b32_e32 v11, v47
	v_add_u32_e32 v12, s16, v4
	v_add_u32_e32 v13, s16, v7
	v_add_u32_e32 v14, s16, v6
	v_add_u32_e32 v15, s16, v5
	s_add_i32 s16, s16, 8
	s_cmp_eq_u32 s16, 0
	s_cselect_b32 s18, 0, s14
	s_cselect_b32 s19, 0, s15
	v_lshl_add_u64 v[2:3], v[2:3], 0, s[18:19]
	global_load_dword v44, v[2:3], off offset:-4096
	global_load_dword v45, v[2:3], off offset:-2048
	global_load_dword v46, v[2:3], off
	global_load_dword v47, v[2:3], off offset:2048
	s_cmp_eq_u32 s16, 0
	v_mul_f32_e32 v16, 0xbfb8aa3b, v8
	v_mul_f32_e32 v17, 0xbfb8aa3b, v9
	v_exp_f32_e32 v16, v16
	v_mul_f32_e32 v18, 0xbfb8aa3b, v10
	v_exp_f32_e32 v17, v17
	v_mul_f32_e32 v19, 0xbfb8aa3b, v11
	v_exp_f32_e32 v18, v18
	v_exp_f32_e32 v19, v19
	v_add_f32_e32 v16, 1.0, v16
	v_add_f32_e32 v17, 1.0, v17
	v_div_scale_f32 v20, s[0:1], v16, v16, v8
	v_add_f32_e32 v18, 1.0, v18
	v_div_scale_f32 v22, s[0:1], v17, v17, v9
	v_rcp_f32_e32 v28, v20
	v_add_f32_e32 v19, 1.0, v19
	v_div_scale_f32 v24, s[2:3], v18, v18, v10
	v_rcp_f32_e32 v29, v22
	v_div_scale_f32 v26, s[4:5], v19, v19, v11
	v_rcp_f32_e32 v30, v24
	v_rcp_f32_e32 v31, v26
	v_fma_f32 v32, -v20, v28, 1.0
	v_div_scale_f32 v21, vcc, v8, v16, v8
	v_fma_f32 v33, -v22, v29, 1.0
	v_fmac_f32_e32 v28, v32, v28
	v_div_scale_f32 v23, s[0:1], v9, v17, v9
	v_fma_f32 v34, -v24, v30, 1.0
	v_fmac_f32_e32 v29, v33, v29
	v_mul_f32_e32 v32, v21, v28
	v_div_scale_f32 v25, s[2:3], v10, v18, v10
	v_fma_f32 v35, -v26, v31, 1.0
	v_fmac_f32_e32 v30, v34, v30
	v_mul_f32_e32 v33, v23, v29
	v_fma_f32 v36, -v20, v32, v21
	v_div_scale_f32 v27, s[4:5], v11, v19, v11
	v_fmac_f32_e32 v31, v35, v31
	v_mul_f32_e32 v34, v25, v30
	v_fma_f32 v37, -v22, v33, v23
	v_fmac_f32_e32 v32, v36, v28
	v_mul_f32_e32 v35, v27, v31
	v_fma_f32 v38, -v24, v34, v25
	v_fmac_f32_e32 v33, v37, v29
	v_fma_f32 v20, -v20, v32, v21
	v_fma_f32 v39, -v26, v35, v27
	v_fmac_f32_e32 v34, v38, v30
	v_fma_f32 v21, -v22, v33, v23
	v_div_fmas_f32 v20, v20, v28, v32
	s_mov_b64 vcc, s[0:1]
	v_fmac_f32_e32 v35, v39, v31
	v_fma_f32 v22, -v24, v34, v25
	v_div_fixup_f32 v8, v20, v16, v8
	v_div_fmas_f32 v16, v21, v29, v33
	s_mov_b64 vcc, s[2:3]
	v_fma_f32 v23, -v26, v35, v27
	ds_write_b32 v12, v8 offset:128
	v_div_fixup_f32 v8, v16, v17, v9
	v_div_fmas_f32 v9, v22, v30, v34
	s_mov_b64 vcc, s[4:5]
	ds_write_b32 v13, v8 offset:128
	v_div_fixup_f32 v8, v9, v18, v10
	v_div_fmas_f32 v9, v23, v31, v35
	ds_write_b32 v14, v8 offset:128
	v_div_fixup_f32 v8, v9, v19, v11
	ds_write_b32 v15, v8 offset:128
	s_cbranch_scc0 .LBB0_10
	s_waitcnt vmcnt(0)
	s_lshl_b32 s0, s58, 6
	s_add_i32 s1, s0, 0xffffe800
	s_cmpk_lt_u32 s58, 0x60
	v_readlane_b32 s17, v252, 46
	s_cselect_b32 s4, s0, s1
	s_lshl_b32 s14, s17, 7
	s_cmpk_gt_u32 s58, 0x5f
	s_cselect_b64 s[0:1], -1, 0
	s_and_b64 s[2:3], s[0:1], exec
	s_cselect_b32 s2, 0x400, 0
	s_add_i32 s2, s2, s14
	s_mov_b32 s5, 0
	s_mul_hi_u32 s14, s2, 0x6000
	s_mul_i32 s15, s2, 0x6000
	s_lshl_b32 s2, s17, 14
	s_add_i32 s17, s2, 0
	s_lshl_b64 s[2:3], s[4:5], 2
	s_mov_b32 s35, s58
	s_add_u32 s5, s15, s2
	v_readlane_b32 s44, v252, 13
	s_addc_u32 s15, s14, s3
	v_readlane_b32 s50, v252, 19
	v_readlane_b32 s51, v252, 20
	s_add_u32 s14, s50, s5
	v_mov_b32_e32 v3, 0
	v_lshlrev_b32_e32 v2, 2, v174
	s_addc_u32 s15, s51, s15
	s_movk_i32 s16, 0x6000
	v_lshl_add_u64 v[4:5], s[14:15], 0, v[2:3]
	s_mov_b64 s[14:15], 0
	s_mov_b32 s5, 0xc000
	s_mov_b32 s18, 0x12000
	v_mov_b32_e32 v6, v3
	v_mov_b32_e32 v7, v3
	v_mov_b32_e32 v8, v3
	v_mov_b32_e32 v9, v3
	v_mov_b32_e32 v10, v3
	v_mov_b32_e32 v11, v3
	v_mov_b32_e32 v12, v3
	v_mov_b32_e32 v13, v3
	v_mov_b32_e32 v14, v3
	v_mov_b32_e32 v15, v3
	v_mov_b32_e32 v16, v3
	v_mov_b32_e32 v17, v3
	v_mov_b32_e32 v18, v3
	v_mov_b32_e32 v19, v3
	v_mov_b32_e32 v20, v3
	v_mov_b32_e32 v21, v3
	v_mov_b32_e32 v22, v3
	v_mov_b32_e32 v23, v3
	v_mov_b32_e32 v24, v3
	v_mov_b32_e32 v25, v3
	v_mov_b32_e32 v26, v3
	v_mov_b32_e32 v27, v3
	v_mov_b32_e32 v28, v3
	v_mov_b32_e32 v29, v3
	v_mov_b32_e32 v30, v3
	v_mov_b32_e32 v31, v3
	v_mov_b32_e32 v32, v3
	v_mov_b32_e32 v33, v3
	v_mov_b32_e32 v34, v3
	v_mov_b32_e32 v35, v3
	v_mov_b32_e32 v36, v3
	v_mov_b32_e32 v37, v3
	s_waitcnt lgkmcnt(0)
	s_barrier
	v_readlane_b32 s45, v252, 14
	v_readlane_b32 s46, v252, 15
	v_readlane_b32 s47, v252, 16
	v_readlane_b32 s48, v252, 17
	v_readlane_b32 s49, v252, 18
	v_readlane_b32 s52, v252, 21
	v_readlane_b32 s53, v252, 22
	v_readlane_b32 s54, v252, 23
	v_readlane_b32 s55, v252, 24
	v_readlane_b32 s56, v252, 25
	v_readlane_b32 s57, v252, 26
	v_readlane_b32 s58, v252, 27
	v_readlane_b32 s59, v252, 28
	s_mov_b32 s25, 0
	s_mov_b32 s24, 0x0
	v_lshl_add_u64 v[210:211], v[4:5], 0, s[24:25]
	v_add_co_u32_e32 v212, vcc, s16, v210
	global_load_dword v178, v[210:211], off
	s_nop 0
	v_addc_co_u32_e32 v213, vcc, 0, v211, vcc
	v_add_co_u32_e32 v214, vcc, s5, v210
	s_nop 1
	v_addc_co_u32_e32 v215, vcc, 0, v211, vcc
	v_add_co_u32_e32 v216, vcc, s18, v210
	s_nop 1
	v_addc_co_u32_e32 v217, vcc, 0, v211, vcc
	global_load_dword v180, v[212:213], off
	global_load_dword v182, v[214:215], off
	global_load_dword v184, v[216:217], off
	s_mov_b32 s24, 0x18000
	v_lshl_add_u64 v[210:211], v[4:5], 0, s[24:25]
	v_add_co_u32_e32 v212, vcc, s16, v210
	global_load_dword v186, v[210:211], off
	s_nop 0
	v_addc_co_u32_e32 v213, vcc, 0, v211, vcc
	v_add_co_u32_e32 v214, vcc, s5, v210
	s_nop 1
	v_addc_co_u32_e32 v215, vcc, 0, v211, vcc
	v_add_co_u32_e32 v216, vcc, s18, v210
	s_nop 1
	v_addc_co_u32_e32 v217, vcc, 0, v211, vcc
	global_load_dword v188, v[212:213], off
	global_load_dword v190, v[214:215], off
	global_load_dword v192, v[216:217], off
	s_mov_b32 s24, 0x30000
	v_lshl_add_u64 v[210:211], v[4:5], 0, s[24:25]
	v_add_co_u32_e32 v212, vcc, s16, v210
	global_load_dword v194, v[210:211], off
	s_nop 0
	v_addc_co_u32_e32 v213, vcc, 0, v211, vcc
	v_add_co_u32_e32 v214, vcc, s5, v210
	s_nop 1
	v_addc_co_u32_e32 v215, vcc, 0, v211, vcc
	v_add_co_u32_e32 v216, vcc, s18, v210
	s_nop 1
	v_addc_co_u32_e32 v217, vcc, 0, v211, vcc
	global_load_dword v196, v[212:213], off
	global_load_dword v198, v[214:215], off
	global_load_dword v200, v[216:217], off

.LBB0_261:
	s_nop 15
	v_mov_b64_e32 v[82:83], v[2:3]
	v_mov_b64_e32 v[66:67], v[18:19]
	v_mov_b64_e32 v[114:115], v[34:35]
	v_mov_b64_e32 v[98:99], v[50:51]
	v_mov_b64_e32 v[84:85], v[4:5]
	v_mov_b64_e32 v[86:87], v[6:7]
	v_mov_b64_e32 v[88:89], v[8:9]
	v_mov_b64_e32 v[90:91], v[10:11]
	v_mov_b64_e32 v[92:93], v[12:13]
	v_mov_b64_e32 v[94:95], v[14:15]
	v_mov_b64_e32 v[96:97], v[16:17]
	v_mov_b64_e32 v[68:69], v[20:21]
	v_mov_b64_e32 v[70:71], v[22:23]
	v_mov_b64_e32 v[72:73], v[24:25]
	v_mov_b64_e32 v[74:75], v[26:27]
	v_mov_b64_e32 v[76:77], v[28:29]
	v_mov_b64_e32 v[78:79], v[30:31]
	v_mov_b64_e32 v[80:81], v[32:33]
	v_mov_b64_e32 v[116:117], v[36:37]
	v_mov_b64_e32 v[118:119], v[38:39]
	v_mov_b64_e32 v[120:121], v[40:41]
	v_mov_b64_e32 v[122:123], v[42:43]
	v_mov_b64_e32 v[124:125], v[44:45]
	v_mov_b64_e32 v[126:127], v[46:47]
	v_mov_b64_e32 v[128:129], v[48:49]
	v_mov_b64_e32 v[100:101], v[52:53]
	v_mov_b64_e32 v[102:103], v[54:55]
	v_mov_b64_e32 v[104:105], v[56:57]
	v_mov_b64_e32 v[106:107], v[58:59]
	v_mov_b64_e32 v[108:109], v[60:61]
	v_mov_b64_e32 v[110:111], v[62:63]
	v_mov_b64_e32 v[112:113], v[64:65]
	s_lshl_b32 s0, s42, 11
	s_or_b32 s0, s0, s78
	v_or_b32_e32 v6, s0, v1
	v_ashrrev_i32_e32 v7, 31, v6
	v_readlane_b32 s92, v253, 0
	v_lshlrev_b64 v[2:3], 11, v[6:7]
	v_readlane_b32 s93, v253, 1
	s_lshl_b32 s42, s76, 1
	v_mov_b32_e32 v193, v177
	v_lshl_add_u64 v[2:3], s[92:93], 0, v[2:3]
	v_lshl_add_u64 v[2:3], v[2:3], 0, s[42:43]
	v_lshl_add_u64 v[8:9], v[2:3], 0, v[192:193]
	v_cvt_pk_bf16_f32 v2, v98, v99
	v_cvt_pk_bf16_f32 v3, v100, v101
	v_cvt_pk_bf16_f32 v4, v102, v103
	v_cvt_pk_bf16_f32 v5, v104, v105
	s_nop 0
	v_permlane32_swap_b32_e32 v2, v4
	v_permlane32_swap_b32_e32 v3, v5
	global_store_dwordx4 v[8:9], v[2:5], off
	v_readlane_b32 s0, v252, 48
	s_add_i32 s75, s75, s0
	v_cvt_pk_bf16_f32 v2, v114, v115
	v_cvt_pk_bf16_f32 v3, v116, v117
	v_cvt_pk_bf16_f32 v4, v118, v119
	v_cvt_pk_bf16_f32 v5, v120, v121
	s_nop 0
	v_permlane32_swap_b32_e32 v2, v4
	v_permlane32_swap_b32_e32 v3, v5
	global_store_dwordx4 v[8:9], v[2:5], off offset:64
	s_add_i32 s64, s64, s0
	s_add_i32 s65, s65, s66
	v_cvt_pk_bf16_f32 v2, v106, v107
	v_cvt_pk_bf16_f32 v3, v108, v109
	v_cvt_pk_bf16_f32 v4, v110, v111
	v_cvt_pk_bf16_f32 v5, v112, v113
	s_nop 0
	v_permlane32_swap_b32_e32 v2, v4
	v_permlane32_swap_b32_e32 v3, v5
	global_store_dwordx4 v[8:9], v[2:5], off offset:32
	v_readlane_b32 s94, v252, 62
	s_cmpk_lt_i32 s75, 0x4000
	v_cvt_pk_bf16_f32 v2, v122, v123
	v_cvt_pk_bf16_f32 v3, v124, v125
	v_cvt_pk_bf16_f32 v4, v126, v127
	v_cvt_pk_bf16_f32 v5, v128, v129
	s_nop 0
	v_permlane32_swap_b32_e32 v2, v4
	v_permlane32_swap_b32_e32 v3, v5
	global_store_dwordx4 v[8:9], v[2:5], off offset:96
	v_readlane_b32 s95, v252, 63
	s_nop 0
	v_or_b32_e32 v2, 32, v6
	v_ashrrev_i32_e32 v3, 31, v2
	v_lshlrev_b64 v[2:3], 11, v[2:3]
	v_lshl_add_u64 v[2:3], s[92:93], 0, v[2:3]
	v_lshl_add_u64 v[2:3], v[2:3], 0, s[42:43]
	v_lshl_add_u64 v[6:7], v[2:3], 0, v[192:193]
	v_cvt_pk_bf16_f32 v2, v66, v67
	v_cvt_pk_bf16_f32 v3, v68, v69
	v_cvt_pk_bf16_f32 v4, v70, v71
	v_cvt_pk_bf16_f32 v5, v72, v73
	s_nop 0
	v_permlane32_swap_b32_e32 v2, v4
	v_permlane32_swap_b32_e32 v3, v5
	global_store_dwordx4 v[6:7], v[2:5], off
	s_nop 1
	v_cvt_pk_bf16_f32 v2, v82, v83
	v_cvt_pk_bf16_f32 v3, v84, v85
	v_cvt_pk_bf16_f32 v4, v86, v87
	v_cvt_pk_bf16_f32 v5, v88, v89
	s_nop 0
	v_permlane32_swap_b32_e32 v2, v4
	v_permlane32_swap_b32_e32 v3, v5
	global_store_dwordx4 v[6:7], v[2:5], off offset:64
	s_nop 1
	v_cvt_pk_bf16_f32 v2, v74, v75
	v_cvt_pk_bf16_f32 v3, v76, v77
	v_cvt_pk_bf16_f32 v4, v78, v79
	v_cvt_pk_bf16_f32 v5, v80, v81
	s_nop 0
	v_permlane32_swap_b32_e32 v2, v4
	v_permlane32_swap_b32_e32 v3, v5
	global_store_dwordx4 v[6:7], v[2:5], off offset:32
	s_nop 1
	v_cvt_pk_bf16_f32 v2, v90, v91
	v_cvt_pk_bf16_f32 v3, v92, v93
	v_cvt_pk_bf16_f32 v4, v94, v95
	v_cvt_pk_bf16_f32 v5, v96, v97
	s_nop 0
	v_permlane32_swap_b32_e32 v2, v4
	v_permlane32_swap_b32_e32 v3, v5
	global_store_dwordx4 v[6:7], v[2:5], off offset:96
	s_waitcnt vmcnt(0)
	s_cbranch_scc0 .LBB0_277

.LBB0_269:
	v_pk_add_f32 v[114:115], v[98:99], 0 op_sel_hi:[1,0]
	v_max_i32_e32 v116, 0, v82
	v_pk_add_f32 v[114:115], v[100:101], v[114:115]
	v_max_i32_e32 v117, 0, v83
	v_pk_add_f32 v[114:115], v[102:103], v[114:115]
	v_max_i32_e32 v118, 0, v84
	v_pk_add_f32 v[114:115], v[104:105], v[114:115]
	v_max_i32_e32 v119, 0, v85
	v_pk_add_f32 v[114:115], v[106:107], v[114:115]
	v_max_i32_e32 v120, 0, v86
	v_pk_add_f32 v[114:115], v[108:109], v[114:115]
	v_max_i32_e32 v121, 0, v87
	v_pk_add_f32 v[114:115], v[110:111], v[114:115]
	v_max_i32_e32 v122, 0, v88
	v_pk_add_f32 v[114:115], v[112:113], v[114:115]
	v_max_i32_e32 v123, 0, v89
	v_pk_add_f32 v[204:205], v[114:115], v[114:115] op_sel:[0,1] op_sel_hi:[1,0]
	v_exp_f32_e64 v114, -|v82|
	v_exp_f32_e64 v115, -|v83|
	v_max_i32_e32 v124, 0, v90
	v_max_i32_e32 v125, 0, v91
	v_max_i32_e32 v126, 0, v92
	v_pk_add_f32 v[114:115], v[114:115], 1.0 op_sel_hi:[1,0]
	v_max_i32_e32 v127, 0, v93
	v_log_f32_e32 v114, v114
	v_log_f32_e32 v115, v115
	v_max_i32_e32 v128, 0, v94
	v_max_i32_e32 v129, 0, v95
	v_max_i32_e32 v208, 0, v96
	v_pk_add_f32 v[114:115], v[114:115], v[116:117]
	v_exp_f32_e64 v116, -|v84|
	v_exp_f32_e64 v117, -|v85|
	v_max_i32_e32 v209, 0, v97
	v_sub_f32_e32 v225, v203, v115
	v_sub_f32_e32 v224, v203, v114
	v_pk_add_f32 v[116:117], v[116:117], 1.0 op_sel_hi:[1,0]
	v_cvt_pk_bf16_f32 v98, v98, v99
	v_log_f32_e32 v116, v116
	v_log_f32_e32 v117, v117
	v_cvt_pk_bf16_f32 v99, v100, v101
	v_cvt_pk_bf16_f32 v100, v102, v103
	v_cvt_pk_bf16_f32 v101, v104, v105
	v_pk_add_f32 v[116:117], v[116:117], v[118:119]
	v_exp_f32_e64 v118, -|v86|
	v_exp_f32_e64 v119, -|v87|
	v_sub_f32_e32 v227, v203, v117
	v_sub_f32_e32 v226, v203, v116
	v_pk_add_f32 v[84:85], v[84:85], v[226:227]
	v_pk_add_f32 v[118:119], v[118:119], 1.0 op_sel_hi:[1,0]
	v_pk_add_f32 v[82:83], v[82:83], v[224:225]
	v_log_f32_e32 v118, v118
	v_log_f32_e32 v119, v119
	v_mfma_f32_32x32x16_bf16 v[66:81], v[130:133], v[98:101], v[66:81]
	v_cvt_pk_bf16_f32 v98, v114, v115
	v_cvt_pk_bf16_f32 v99, v116, v117
	v_add_f32_e64 v118, v118, v120
	v_add_f32_e64 v119, v119, v121
	v_exp_f32_e64 v120, -|v88|
	v_exp_f32_e64 v121, -|v89|
	v_sub_f32_e32 v229, v203, v119
	v_sub_f32_e32 v228, v203, v118
	v_pk_add_f32 v[86:87], v[86:87], v[228:229]
	v_pk_add_f32 v[120:121], v[120:121], 1.0 op_sel_hi:[1,0]
	v_cvt_pk_bf16_f32 v100, v118, v119
	v_log_f32_e32 v120, v120
	v_log_f32_e32 v121, v121
	v_add_u32_e32 v244, s81, v210
	v_mov_b32_e32 v206, v204
	s_nop 1
	v_permlane32_swap_b32_e32 v204, v206
	v_pk_add_f32 v[122:123], v[120:121], v[122:123]
	v_exp_f32_e64 v120, -|v90|
	v_exp_f32_e64 v121, -|v91|
	v_sub_f32_e32 v231, v203, v123
	v_sub_f32_e32 v230, v203, v122
	v_pk_add_f32 v[88:89], v[88:89], v[230:231]
	v_pk_add_f32 v[120:121], v[120:121], 1.0 op_sel_hi:[1,0]
	v_cvt_pk_bf16_f32 v101, v122, v123
	v_log_f32_e32 v120, v120
	v_log_f32_e32 v121, v121
	s_nop 0
	v_pk_add_f32 v[120:121], v[120:121], v[124:125]
	v_exp_f32_e64 v124, -|v92|
	v_exp_f32_e64 v125, -|v93|
	v_sub_f32_e32 v233, v203, v121
	v_sub_f32_e32 v232, v203, v120
	v_pk_add_f32 v[90:91], v[90:91], v[232:233]
	v_pk_add_f32 v[124:125], v[124:125], 1.0 op_sel_hi:[1,0]
	s_nop 0
	v_log_f32_e32 v124, v124
	v_log_f32_e32 v125, v125
	s_nop 0
	v_pk_add_f32 v[124:125], v[124:125], v[126:127]
	v_exp_f32_e64 v126, -|v94|
	v_exp_f32_e64 v127, -|v95|
	v_sub_f32_e32 v235, v203, v125
	v_sub_f32_e32 v234, v203, v124
	v_pk_add_f32 v[92:93], v[92:93], v[234:235]
	v_pk_add_f32 v[126:127], v[126:127], 1.0 op_sel_hi:[1,0]
	s_nop 0
	v_log_f32_e32 v126, v126
	v_log_f32_e32 v127, v127
	s_nop 0
	v_pk_add_f32 v[126:127], v[126:127], v[128:129]
	v_exp_f32_e64 v128, -|v96|
	v_exp_f32_e64 v129, -|v97|
	v_sub_f32_e32 v237, v203, v127
	v_sub_f32_e32 v236, v203, v126
	v_pk_add_f32 v[94:95], v[94:95], v[236:237]
	v_pk_add_f32 v[128:129], v[128:129], 1.0 op_sel_hi:[1,0]
	s_nop 0
	v_log_f32_e32 v128, v128
	v_log_f32_e32 v129, v129
	s_nop 0
	v_pk_add_f32 v[128:129], v[128:129], v[208:209]
	s_nop 0
	v_sub_f32_e32 v239, v203, v129
	v_sub_f32_e32 v238, v203, v128
	v_pk_add_f32 v[96:97], v[96:97], v[238:239]
	v_pk_add_f32 v[208:209], v[114:115], v[116:117]
	s_nop 0
	v_mfma_f32_32x32x16_bf16 v[82:97], v[130:133], v[98:101], v[82:97]
	v_cvt_pk_bf16_f32 v98, v106, v107
	v_cvt_pk_bf16_f32 v99, v108, v109
	v_cvt_pk_bf16_f32 v100, v110, v111
	v_cvt_pk_bf16_f32 v101, v112, v113
	v_add_f32_e64 v208, v118, v208
	v_add_f32_e64 v209, v119, v209
	v_pk_add_f32 v[208:209], v[122:123], v[208:209]
	v_mfma_f32_32x32x16_bf16 v[66:81], v[134:137], v[98:101], v[66:81]
	v_cvt_pk_bf16_f32 v98, v120, v121
	v_cvt_pk_bf16_f32 v99, v124, v125
	v_cvt_pk_bf16_f32 v100, v126, v127
	v_cvt_pk_bf16_f32 v101, v128, v129
	v_add_f32_e64 v208, v120, v208
	v_add_f32_e64 v209, v121, v209
	s_nop 5
	v_exp_f32_e32 v66, v66
	v_mfma_f32_32x32x16_bf16 v[82:97], v[134:137], v[98:101], v[82:97]
	v_add_f32_e64 v208, v124, v208
	v_add_f32_e64 v209, v125, v209
	v_exp_f32_e32 v67, v67
	v_pk_add_f32 v[208:209], v[126:127], v[208:209]
	v_exp_f32_e32 v68, v68
	v_exp_f32_e32 v69, v69
	v_exp_f32_e32 v70, v70
	v_exp_f32_e32 v71, v71
	s_nop 3
	v_exp_f32_e32 v86, v86
	v_exp_f32_e32 v87, v87
	v_exp_f32_e32 v88, v88
	v_exp_f32_e32 v89, v89
	v_exp_f32_e32 v98, v82
	v_exp_f32_e32 v99, v83
	v_exp_f32_e32 v100, v84
	v_exp_f32_e32 v101, v85
	v_exp_f32_e32 v72, v72
	v_exp_f32_e32 v73, v73
	v_cvt_pk_bf16_f32 v226, v86, v87
	v_cvt_pk_bf16_f32 v227, v88, v89
	s_nop 0
	ds_read_b64_tr_b16 v[86:87], v244 offset:4096
	ds_read_b64_tr_b16 v[88:89], v244 offset:5120
	ds_read_b64_tr_b16 v[228:229], v244 offset:4608
	ds_read_b64_tr_b16 v[230:231], v244 offset:5632
	v_pk_add_f32 v[208:209], v[128:129], v[208:209]
	v_exp_f32_e32 v205, v90
	v_exp_f32_e32 v223, v91
	v_pk_add_f32 v[208:209], v[208:209], v[208:209] op_sel:[0,1] op_sel_hi:[1,0]
	v_exp_f32_e32 v232, v76
	v_mov_b32_e32 v207, v208
	s_nop 1
	v_permlane32_swap_b32_e32 v208, v207
	v_exp_f32_e32 v233, v92
	v_exp_f32_e32 v234, v77
	v_exp_f32_e32 v235, v93
	v_exp_f32_e32 v236, v78
	v_exp_f32_e32 v237, v94
	v_exp_f32_e32 v238, v79
	v_exp_f32_e32 v239, v95
	v_cvt_pk_bf16_f32 v82, v66, v67
	v_cvt_pk_bf16_f32 v83, v68, v69
	v_cvt_pk_bf16_f32 v84, v70, v71
	v_cvt_pk_bf16_f32 v85, v72, v73
	v_cvt_pk_bf16_f32 v224, v98, v99
	v_cvt_pk_bf16_f32 v225, v100, v101
	v_exp_f32_e32 v175, v74
	v_exp_f32_e32 v209, v75
	v_exp_f32_e32 v240, v80
	v_exp_f32_e32 v241, v96
	v_exp_f32_e32 v242, v81
	v_exp_f32_e32 v243, v97
	s_waitcnt lgkmcnt(2)
	v_mfma_f32_32x32x16_bf16 v[50:65], v[86:89], v[82:85], v[50:65]
	v_mfma_f32_32x32x16_bf16 v[18:33], v[86:89], v[224:227], v[18:33]
	s_waitcnt lgkmcnt(0)
	v_mfma_f32_32x32x16_bf16 v[34:49], v[228:231], v[82:85], v[34:49]
	v_mfma_f32_32x32x16_bf16 v[2:17], v[228:231], v[224:227], v[2:17]
	v_cvt_pk_bf16_f32 v228, v205, v223
	v_mov_b32_e32 v205, v208
	v_add_f32_e64 v204, v204, v206
	v_add_f32_e64 v205, v205, v207
	v_cvt_pk_bf16_f32 v225, v232, v234
	v_pk_add_f32 v[204:205], v[202:203], v[204:205] neg_lo:[0,1] neg_hi:[0,1]
	v_cvt_pk_bf16_f32 v226, v236, v238
	v_cvt_pk_bf16_f32 v229, v233, v235
	v_cvt_pk_bf16_f32 v230, v237, v239
	ds_read_b64_tr_b16 v[232:233], v244 offset:6144
	ds_read_b64_tr_b16 v[234:235], v244 offset:7168
	ds_read_b64_tr_b16 v[236:237], v244 offset:6656
	ds_read_b64_tr_b16 v[238:239], v244 offset:7680
	v_cmp_gt_f32_e32 vcc, s72, v204
	v_cmp_gt_f32_e64 s[0:1], s72, v205
	s_and_b64 s[0:1], vcc, s[0:1]
	v_cvt_pk_bf16_f32 v224, v175, v209
	v_cndmask_b32_e64 v175, 0, 1, s[0:1]
	v_cmp_ne_u32_e32 vcc, 0, v175
	v_cvt_pk_bf16_f32 v227, v240, v242
	v_cvt_pk_bf16_f32 v231, v241, v243
	s_cmp_lg_u64 vcc, exec
	s_waitcnt lgkmcnt(2)
	v_mfma_f32_32x32x16_bf16 v[50:65], v[232:235], v[224:227], v[50:65]
	s_cselect_b64 s[0:1], -1, 0
	v_mfma_f32_32x32x16_bf16 v[18:33], v[232:235], v[228:231], v[18:33]
	s_waitcnt lgkmcnt(0)
	v_mfma_f32_32x32x16_bf16 v[34:49], v[236:239], v[224:227], v[34:49]
	v_mfma_f32_32x32x16_bf16 v[2:17], v[236:239], v[228:231], v[2:17]
	s_branch .LBB0_271

.LBB0_273:
	s_cmp_lg_u32 s80, 0
	s_cselect_b64 s[36:37], -1, 0
	s_and_b64 s[0:1], s[0:1], s[36:37]
	s_add_u32 s56, s56, 0xfffd0000
	s_addc_u32 s57, s57, -1
	v_add_u32_e32 v176, 0xfffe8000, v176
	s_and_b64 vcc, exec, s[0:1]
	s_cbranch_vccz .LBB0_261
	v_mov_b64_e32 v[202:203], v[204:205]
	s_branch .LBB0_263
